# attention inner loop heads aligned to 64 bytes (p2align 6); otherwise as v19
# speedup vs baseline: 1.0032x; 1.0032x over previous
.LBB0_756:
	s_and_b32 s8, s8, 7
	s_ashr_i32 s31, s30, 31
	s_mul_i32 s7, s30, 0xc00
	s_mul_hi_i32 s6, s30, 0xc00
	s_add_u32 s7, s37, s7
	s_addc_u32 s6, s38, s6
	s_mul_i32 s9, s8, 0x180
	s_add_u32 s10, s7, s9
	s_addc_u32 s11, s6, 0
	s_add_u32 s6, s39, s9
	s_addc_u32 s7, s40, 0
	s_lshl_b32 s61, s8, 7
	s_lshl_b32 s8, s8, 8
	s_add_u32 s34, s41, s8
	v_readfirstlane_b32 s9, v254
	s_addc_u32 s35, s42, 0
	s_ashr_i32 s8, s9, 6
	s_lshl_b32 s82, s8, 10
	s_mov_b32 s72, s6
	s_and_b32 s73, s7, 0xffff
	s_mov_b32 s74, 0x7ffffff0
	s_mov_b32 s75, 0x20000
	s_mov_b32 s76, s34
	s_and_b32 s77, s35, 0xffff
	s_mov_b32 s78, 0x7ffffff0
	s_mov_b32 s79, 0x20000
	v_lshl_or_b32 v2, s8, 5, v188
	v_mov_b64_e32 v[0:1], s[10:11]
	v_mad_i64_i32 v[0:1], s[10:11], v2, s46, v[0:1]
	v_lshl_add_u64 v[26:27], s[26:27], 0, v[142:143]
	v_lshl_add_u64 v[28:29], v[146:147], 0, s[26:27]
	v_lshl_add_u64 v[38:39], v[0:1], 0, v[148:149]
	v_lshlrev_b64 v[0:1], 11, v[26:27]
	v_lshlrev_b64 v[18:19], 11, v[28:29]
	v_lshl_add_u64 v[0:1], s[34:35], 0, v[0:1]
	v_lshl_add_u64 v[18:19], s[34:35], 0, v[18:19]
	v_lshl_add_u64 v[0:1], v[0:1], 0, v[150:151]
	v_lshl_add_u64 v[22:23], v[18:19], 0, v[150:151]
	global_load_dwordx4 v[2:5], v[38:39], off offset:256
	global_load_dwordx4 v[6:9], v[38:39], off offset:288
	global_load_dwordx4 v[10:13], v[38:39], off offset:320
	global_load_dwordx4 v[14:17], v[38:39], off offset:352
	global_load_dwordx4 v[18:21], v[0:1], off
	s_nop 0
	global_load_dwordx4 v[22:25], v[22:23], off
	v_mov_b64_e32 v[0:1], s[6:7]
	v_mad_u64_u32 v[30:31], s[10:11], v26, s46, v[0:1]
	v_mad_i32_i24 v31, v27, s46, v31
	v_lshl_add_u64 v[26:27], v[30:31], 0, v[150:151]
	v_mad_u64_u32 v[30:31], s[10:11], v28, s46, v[0:1]
	v_mad_i32_i24 v31, v29, s46, v31
	v_lshl_add_u64 v[30:31], v[30:31], 0, v[150:151]
	v_lshl_add_u64 v[34:35], s[26:27], 0, v[144:145]
	global_load_dwordx4 v[26:29], v[26:27], off
	s_nop 0
	global_load_dwordx4 v[30:33], v[30:31], off
	v_mad_u64_u32 v[36:37], s[10:11], v34, s46, v[0:1]
	v_mad_i32_i24 v37, v35, s46, v37
	v_lshl_add_u64 v[34:35], v[36:37], 0, v[152:153]
	global_load_dwordx4 v[34:37], v[34:35], off offset:256
	s_nop 0
	global_load_dwordx4 v[124:127], v[38:39], off
	global_load_dwordx4 v[120:123], v[38:39], off offset:32
	global_load_dwordx4 v[116:119], v[38:39], off offset:64
	global_load_dwordx4 v[112:115], v[38:39], off offset:96
	global_load_dwordx4 v[108:111], v[38:39], off offset:128
	global_load_dwordx4 v[104:107], v[38:39], off offset:160
	global_load_dwordx4 v[100:103], v[38:39], off offset:192
	global_load_dwordx4 v[96:99], v[38:39], off offset:224
	s_lshl_b32 s8, s8, 12
	v_add_u32_e32 v190, s8, v166
	v_add_u32_e32 v191, s47, v170
	v_add_u32_e32 v192, s47, v171
	v_add_u32_e32 v193, s47, v172
	v_add_u32_e32 v194, s47, v173
	s_and_b32 s9, s9, 0x3fffffc0
	s_lshl_b32 s9, s9, 2
	s_add_i32 s62, s9, 0
	s_add_i32 s62, s62, 0x14000
	s_mov_b32 s11, s27
	s_mov_b32 s22, s27
	s_mov_b32 s23, s27
	s_mov_b32 s8, s27
	s_mov_b32 s9, s27
	s_mov_b32 s12, s27
	s_mov_b32 s13, s27
	s_mov_b32 s14, s27
	s_mov_b32 s15, s27
	s_mov_b32 s16, s27
	s_mov_b32 s17, s27
	s_mov_b32 s18, s27
	s_mov_b32 s19, s27
	s_mov_b32 s20, s27
	s_mov_b32 s21, s27
	v_add_u32_e32 v195, 0, v168
	s_mov_b32 s64, 2
	v_mov_b32_e32 v140, 0
	v_add_u32_e32 v196, 0x12000, v195
	v_lshrrev_b32_e32 v156, 4, v254
	v_and_b32_e32 v157, 7, v156
	v_and_b32_e32 v159, 15, v254
	v_xor_b32_e32 v157, v157, v159
	v_lshlrev_b32_e32 v157, 4, v157
	v_mad_u32_u24 v154, v156, s46, v157
	v_lshrrev_b32_e32 v156, 3, v254
	v_and_b32_e32 v157, 7, v156
	v_and_b32_e32 v159, 7, v254
	v_xor_b32_e32 v157, v157, v159
	v_lshlrev_b32_e32 v157, 4, v157
	v_add_u32_e32 v157, 0x100, v157
	v_mad_u32_u24 v155, v156, s46, v157
	v_and_b32_e32 v158, 3, v254
	v_lshlrev_b32_e32 v158, 4, v158
	v_bfe_u32 v156, v254, 5, 2
	v_lshl_or_b32 v158, v156, 6, v158
	v_bfe_u32 v156, v254, 2, 2
	v_lshl_or_b32 v158, v156, 11, v158
	v_bfe_u32 v156, v254, 7, 1
	v_lshl_or_b32 v158, v156, 13, v158
	v_bfe_u32 v156, v254, 4, 1
	v_lshl_or_b32 v158, v156, 14, v158
	v_bfe_u32 v156, v254, 8, 1
	v_lshl_or_b32 v158, v156, 15, v158
	v_lshl_add_u32 v189, v188, 2, s62
	s_waitcnt vmcnt(16)
	ds_write_b128 v190, v[2:5]
	s_waitcnt vmcnt(15)
	ds_write_b128 v190, v[6:9] offset:1024
	s_waitcnt vmcnt(14)
	ds_write_b128 v190, v[10:13] offset:2048
	s_waitcnt vmcnt(13)
	ds_write_b128 v190, v[14:17] offset:3072
	s_waitcnt vmcnt(0)
	s_waitcnt vmcnt(12)
	ds_write_b128 v175, v[18:21]
	s_waitcnt vmcnt(11)
	ds_write_b128 v176, v[22:25]
	s_waitcnt vmcnt(10)
	ds_write_b128 v177, v[26:29] offset:32768
	s_waitcnt vmcnt(9)
	ds_write_b128 v178, v[30:33] offset:32768
	s_waitcnt vmcnt(8)
	ds_write_b128 v179, v[34:37]
	s_waitcnt lgkmcnt(0)
	s_barrier
	ds_read_b128 v[2:5], v180 offset:32768
	ds_read_b128 v[6:9], v180 offset:40960
	s_waitcnt vmcnt(7) lgkmcnt(1)
	v_mfma_f32_32x32x16_bf16 v[48:63], v[2:5], v[124:127], 0
	s_waitcnt lgkmcnt(0)
	v_mfma_f32_32x32x16_bf16 v[64:79], v[6:9], v[124:127], 0
	ds_read_b128 v[2:5], v181 offset:32768
	ds_read_b128 v[6:9], v181 offset:40960
	s_waitcnt vmcnt(6) lgkmcnt(1)
	v_mfma_f32_32x32x16_bf16 v[48:63], v[2:5], v[120:123], v[48:63]
	s_waitcnt lgkmcnt(0)
	v_mfma_f32_32x32x16_bf16 v[64:79], v[6:9], v[120:123], v[64:79]
	ds_read_b128 v[2:5], v182 offset:32768
	ds_read_b128 v[6:9], v182 offset:40960
	s_waitcnt vmcnt(5) lgkmcnt(1)
	v_mfma_f32_32x32x16_bf16 v[48:63], v[2:5], v[116:119], v[48:63]
	s_waitcnt lgkmcnt(0)
	v_mfma_f32_32x32x16_bf16 v[64:79], v[6:9], v[116:119], v[64:79]
	ds_read_b128 v[2:5], v183 offset:32768
	ds_read_b128 v[6:9], v183 offset:40960
	s_waitcnt vmcnt(4) lgkmcnt(1)
	v_mfma_f32_32x32x16_bf16 v[48:63], v[2:5], v[112:115], v[48:63]
	s_waitcnt lgkmcnt(0)
	v_mfma_f32_32x32x16_bf16 v[64:79], v[6:9], v[112:115], v[64:79]
	ds_read_b128 v[2:5], v184 offset:32768
	ds_read_b128 v[6:9], v184 offset:40960
	s_waitcnt vmcnt(3) lgkmcnt(1)
	v_mfma_f32_32x32x16_bf16 v[48:63], v[2:5], v[108:111], v[48:63]
	s_waitcnt lgkmcnt(0)
	v_mfma_f32_32x32x16_bf16 v[64:79], v[6:9], v[108:111], v[64:79]
	ds_read_b128 v[2:5], v185 offset:32768
	ds_read_b128 v[6:9], v185 offset:40960
	s_waitcnt vmcnt(2) lgkmcnt(1)
	v_mfma_f32_32x32x16_bf16 v[48:63], v[2:5], v[104:107], v[48:63]
	s_waitcnt lgkmcnt(0)
	v_mfma_f32_32x32x16_bf16 v[64:79], v[6:9], v[104:107], v[64:79]
	ds_read_b128 v[2:5], v186 offset:32768
	ds_read_b128 v[6:9], v186 offset:40960
	s_waitcnt vmcnt(1) lgkmcnt(1)
	v_mfma_f32_32x32x16_bf16 v[48:63], v[2:5], v[100:103], v[48:63]
	s_waitcnt lgkmcnt(0)
	v_mfma_f32_32x32x16_bf16 v[64:79], v[6:9], v[100:103], v[64:79]
	ds_read_b128 v[2:5], v187 offset:32768
	ds_read_b128 v[6:9], v187 offset:40960
	s_waitcnt vmcnt(0) lgkmcnt(1)
	v_mfma_f32_32x32x16_bf16 v[48:63], v[2:5], v[96:99], v[48:63]
	s_waitcnt lgkmcnt(0)
	v_mfma_f32_32x32x16_bf16 v[64:79], v[6:9], v[96:99], v[64:79]
	ds_read_b128 v[2:5], v191
	ds_read_b128 v[6:9], v190
	ds_read_b128 v[10:13], v191 offset:4096
	ds_read_b128 v[14:17], v190 offset:1024
	s_waitcnt lgkmcnt(2)
	v_mfma_f32_32x32x16_bf16 v[48:63], v[2:5], v[6:9], v[48:63]
	s_waitcnt lgkmcnt(1)
	v_mfma_f32_32x32x16_bf16 v[64:79], v[10:13], v[6:9], v[64:79]
	ds_read_b128 v[2:5], v192
	ds_read_b128 v[6:9], v192 offset:4096
	s_waitcnt lgkmcnt(1)
	v_mfma_f32_32x32x16_bf16 v[48:63], v[2:5], v[14:17], v[48:63]
	s_waitcnt lgkmcnt(0)
	v_mfma_f32_32x32x16_bf16 v[64:79], v[6:9], v[14:17], v[64:79]
	ds_read_b128 v[2:5], v193
	ds_read_b128 v[6:9], v190 offset:2048
	ds_read_b128 v[10:13], v193 offset:4096
	ds_read_b128 v[14:17], v190 offset:3072
	s_waitcnt lgkmcnt(2)
	v_mfma_f32_32x32x16_bf16 v[48:63], v[2:5], v[6:9], v[48:63]
	s_waitcnt lgkmcnt(1)
	v_mfma_f32_32x32x16_bf16 v[64:79], v[10:13], v[6:9], v[64:79]
	ds_read_b128 v[2:5], v194
	ds_read_b128 v[6:9], v194 offset:4096
	s_waitcnt lgkmcnt(1)
	v_mfma_f32_32x32x16_bf16 v[48:63], v[2:5], v[14:17], v[48:63]
	s_waitcnt lgkmcnt(0)
	v_mfma_f32_32x32x16_bf16 v[64:79], v[6:9], v[14:17], v[64:79]
	s_nop 9
	v_max_f32_e32 v2, v49, v49
	v_max_f32_e32 v3, v48, v48
	v_max_f32_e32 v2, v3, v2
	v_max3_f32 v2, v2, v50, v51
	v_max3_f32 v2, v2, v52, v53
	v_max3_f32 v2, v2, v54, v55
	v_max3_f32 v2, v2, v56, v57
	v_max3_f32 v2, v2, v58, v59
	v_max3_f32 v2, v2, v60, v61
	v_max3_f32 v2, v2, v62, v63
	v_max3_f32 v2, v2, v64, v65
	v_max3_f32 v2, v2, v66, v67
	v_max3_f32 v2, v2, v68, v69
	v_max3_f32 v2, v2, v70, v71
	v_max3_f32 v2, v2, v72, v73
	v_max3_f32 v2, v2, v74, v75
	v_max3_f32 v2, v2, v76, v77
	v_max3_f32 v2, v2, v78, v79
	v_mov_b32_e32 v3, v2
	s_nop 1
	v_permlane32_swap_b32_e32 v2, v3
	v_max_f32_e32 v3, v3, v3
	v_max_f32_e32 v2, v2, v2
	v_max_f32_e32 v2, v2, v3
	v_add_f32_e32 v3, 0x7149f2ca, v2
	v_cmp_ge_f32_e32 vcc, s48, v3
	s_cmp_eq_u64 vcc, exec
	s_cselect_b64 vcc, -1, 0
	s_add_i32 s10, s26, 64
	v_max_f32_e32 v128, 0xf149f2ca, v2
	v_lshl_add_u64 v[2:3], s[10:11], 0, v[142:143]
	v_lshl_add_u64 v[4:5], v[146:147], 0, s[10:11]
	v_lshl_add_u64 v[6:7], s[10:11], 0, v[144:145]
	v_lshlrev_b64 v[8:9], 11, v[2:3]
	v_lshlrev_b64 v[10:11], 11, v[4:5]
	v_mad_u64_u32 v[12:13], s[10:11], v2, s46, v[0:1]
	v_mad_u64_u32 v[14:15], s[10:11], v4, s46, v[0:1]
	v_mad_u64_u32 v[0:1], s[10:11], v6, s46, v[0:1]
	v_lshl_add_u64 v[8:9], s[34:35], 0, v[8:9]
	v_lshl_add_u64 v[10:11], s[34:35], 0, v[10:11]
	v_mad_i32_i24 v13, v3, s46, v13
	v_mad_i32_i24 v15, v5, s46, v15
	v_mad_i32_i24 v1, v7, s46, v1
	v_lshl_add_u64 v[2:3], v[8:9], 0, v[150:151]
	v_lshl_add_u64 v[4:5], v[10:11], 0, v[150:151]
	v_lshl_add_u64 v[6:7], v[12:13], 0, v[150:151]
	v_lshl_add_u64 v[8:9], v[14:15], 0, v[150:151]
	v_lshl_add_u64 v[0:1], v[0:1], 0, v[152:153]
	global_load_dwordx4 v[80:83], v[2:3], off
	global_load_dwordx4 v[84:87], v[4:5], off
	global_load_dwordx4 v[88:91], v[6:7], off
	global_load_dwordx4 v[92:95], v[8:9], off
	global_load_dwordx4 v[200:203], v[0:1], off offset:256
	v_sub_f32_e32 v129, 0xf149f2ca, v128
	v_mul_f32_e32 v129, 0x3dd53b94, v129
	v_exp_f32_e32 v164, v129
	v_mov_b32_e32 v129, 0xf149f2ca
	v_cndmask_b32_e32 v198, v128, v129, vcc
	v_mul_f32_e32 v138, 0xbdd53b94, v198
	v_mov_b32_e32 v165, v138
	v_fmamk_f32 v48, v48, 0x3dd53b94, v138
	v_fmamk_f32 v49, v49, 0x3dd53b94, v138
	v_fmamk_f32 v50, v50, 0x3dd53b94, v138
	v_fmamk_f32 v51, v51, 0x3dd53b94, v138
	v_fmamk_f32 v52, v52, 0x3dd53b94, v138
	v_fmamk_f32 v53, v53, 0x3dd53b94, v138
	v_fmamk_f32 v54, v54, 0x3dd53b94, v138
	v_fmamk_f32 v55, v55, 0x3dd53b94, v138
	v_fmamk_f32 v56, v56, 0x3dd53b94, v138
	v_fmamk_f32 v57, v57, 0x3dd53b94, v138
	v_fmamk_f32 v58, v58, 0x3dd53b94, v138
	v_fmamk_f32 v59, v59, 0x3dd53b94, v138
	v_fmamk_f32 v60, v60, 0x3dd53b94, v138
	v_fmamk_f32 v61, v61, 0x3dd53b94, v138
	v_fmamk_f32 v62, v62, 0x3dd53b94, v138
	v_fmac_f32_e32 v165, 0x3dd53b94, v63
	s_mov_b32 s10, s27
	s_mov_b32 s11, s27
	v_mov_b64_e32 v[30:31], s[22:23]
	v_exp_f32_e32 v222, v48
	v_exp_f32_e32 v224, v49
	v_exp_f32_e32 v220, v50
	v_exp_f32_e32 v223, v51
	v_exp_f32_e32 v219, v52
	v_exp_f32_e32 v221, v53
	v_exp_f32_e32 v217, v54
	v_exp_f32_e32 v218, v55
	v_exp_f32_e32 v212, v56
	v_exp_f32_e32 v214, v57
	v_exp_f32_e32 v211, v58
	v_exp_f32_e32 v213, v59
	v_exp_f32_e32 v208, v60
	v_exp_f32_e32 v210, v61
	v_exp_f32_e32 v207, v62
	v_exp_f32_e32 v209, v165
	v_mov_b64_e32 v[16:17], s[8:9]
	s_waitcnt vmcnt(0)
	v_mov_b64_e32 v[28:29], s[20:21]
	v_mov_b64_e32 v[26:27], s[18:19]
	v_mov_b64_e32 v[24:25], s[16:17]
	v_mov_b64_e32 v[22:23], s[14:15]
	v_mov_b64_e32 v[20:21], s[12:13]
	v_mov_b64_e32 v[18:19], s[10:11]
	v_mov_b64_e32 v[46:47], v[30:31]
	v_mov_b64_e32 v[0:1], v[16:17]
	v_mov_b64_e32 v[62:63], v[30:31]
	v_mov_b64_e32 v[44:45], v[28:29]
	v_mov_b64_e32 v[42:43], v[26:27]
	v_mov_b64_e32 v[40:41], v[24:25]
	v_mov_b64_e32 v[38:39], v[22:23]
	v_mov_b64_e32 v[36:37], v[20:21]
	v_mov_b64_e32 v[34:35], v[18:19]
	v_mov_b64_e32 v[32:33], v[16:17]
	v_mov_b64_e32 v[2:3], v[18:19]
	v_mov_b64_e32 v[4:5], v[20:21]
	v_mov_b64_e32 v[6:7], v[22:23]
	v_mov_b64_e32 v[8:9], v[24:25]
	v_mov_b64_e32 v[10:11], v[26:27]
	v_mov_b64_e32 v[12:13], v[28:29]
	v_mov_b64_e32 v[14:15], v[30:31]
	s_add_i32 s10, s26, 0x80
	s_add_i32 s83, s26, 64
	s_sub_i32 s11, s65, 64
	v_pk_fma_f32 v[134:135], v[78:79], s[28:29], v[138:139] op_sel_hi:[1,0,0]
	v_pk_fma_f32 v[160:161], v[76:77], s[28:29], v[138:139] op_sel_hi:[1,0,0]
	v_pk_fma_f32 v[162:163], v[74:75], s[28:29], v[138:139] op_sel_hi:[1,0,0]
	v_pk_fma_f32 v[128:129], v[72:73], s[28:29], v[138:139] op_sel_hi:[1,0,0]
	v_pk_fma_f32 v[130:131], v[70:71], s[28:29], v[138:139] op_sel_hi:[1,0,0]
	v_pk_fma_f32 v[132:133], v[68:69], s[28:29], v[138:139] op_sel_hi:[1,0,0]
	v_pk_fma_f32 v[136:137], v[66:67], s[28:29], v[138:139] op_sel_hi:[1,0,0]
	v_pk_fma_f32 v[138:139], v[64:65], s[28:29], v[138:139] op_sel_hi:[1,0,0]
	v_cndmask_b32_e64 v197, v164, 1.0, vcc
	v_mov_b64_e32 v[60:61], v[28:29]
	v_mov_b64_e32 v[58:59], v[26:27]
	v_mov_b64_e32 v[56:57], v[24:25]
	v_mov_b64_e32 v[54:55], v[22:23]
	v_mov_b64_e32 v[52:53], v[20:21]
	v_mov_b64_e32 v[50:51], v[18:19]
	v_mov_b64_e32 v[48:49], v[16:17]
	s_waitcnt vmcnt(4)
	ds_write_b128 v175, v[80:83] offset:16384
	s_waitcnt vmcnt(3)
	ds_write_b128 v176, v[84:87] offset:16384
	s_waitcnt vmcnt(2)
	ds_write_b128 v177, v[88:91] offset:49152
	s_waitcnt vmcnt(1)
	ds_write_b128 v178, v[92:95] offset:49152
	s_waitcnt vmcnt(0)
	ds_write_b128 v196, v[200:203]
	s_waitcnt lgkmcnt(0)
	s_barrier
	.p2align	6

.LBB0_2011:
	s_ashr_i32 s6, s11, 3
	s_lshl_b32 s60, s6, 8
	s_lshl_b32 s61, s6, 12
	s_lshl_b32 s6, s10, 8
	s_and_b32 s6, s6, 0xf00
	s_or_b32 s28, s61, s6
	s_add_i32 s8, s60, 0x4000
	s_and_b32 s12, s11, 7
	s_ashr_i32 s29, s28, 31
	s_mul_i32 s7, s28, 0xc00
	s_mul_hi_i32 s6, s28, 0xc00
	s_add_u32 s7, s35, s7
	s_addc_u32 s6, s36, s6
	s_mul_i32 s13, s12, 0x180
	s_add_u32 s10, s7, s13
	s_addc_u32 s11, s6, 0
	s_add_u32 s6, s37, s13
	s_addc_u32 s7, s38, 0
	s_lshl_b32 s59, s12, 7
	s_lshl_b32 s12, s12, 8
	s_add_u32 s30, s39, s12
	v_readfirstlane_b32 s62, v254
	s_addc_u32 s31, s40, 0
	s_ashr_i32 s12, s62, 6
	s_lshl_b32 s82, s12, 10
	s_mov_b32 s72, s6
	s_and_b32 s73, s7, 0xffff
	s_mov_b32 s74, 0x7ffffff0
	s_mov_b32 s75, 0x20000
	s_mov_b32 s76, s30
	s_and_b32 s77, s31, 0xffff
	s_mov_b32 s78, 0x7ffffff0
	s_mov_b32 s79, 0x20000
	v_lshl_add_u64 v[26:27], s[8:9], 0, v[142:143]
	v_lshl_add_u64 v[28:29], v[146:147], 0, s[8:9]
	v_lshl_or_b32 v2, s12, 5, v188
	v_mov_b64_e32 v[0:1], s[10:11]
	v_lshlrev_b64 v[16:17], 11, v[26:27]
	v_lshlrev_b64 v[18:19], 11, v[28:29]
	v_mad_i64_i32 v[0:1], s[10:11], v2, s44, v[0:1]
	v_lshl_add_u64 v[16:17], s[30:31], 0, v[16:17]
	v_lshl_add_u64 v[18:19], s[30:31], 0, v[18:19]
	v_lshl_add_u64 v[38:39], v[0:1], 0, v[148:149]
	v_lshl_add_u64 v[16:17], v[16:17], 0, v[150:151]
	v_lshl_add_u64 v[22:23], v[18:19], 0, v[150:151]
	global_load_dwordx4 v[0:3], v[38:39], off offset:256
	global_load_dwordx4 v[4:7], v[38:39], off offset:288
	global_load_dwordx4 v[8:11], v[38:39], off offset:320
	global_load_dwordx4 v[12:15], v[38:39], off offset:352
	global_load_dwordx4 v[18:21], v[16:17], off
	s_nop 0
	global_load_dwordx4 v[22:25], v[22:23], off
	v_mov_b64_e32 v[16:17], s[6:7]
	v_mad_u64_u32 v[30:31], s[10:11], v26, s44, v[16:17]
	v_mad_i32_i24 v31, v27, s44, v31
	v_lshl_add_u64 v[26:27], v[30:31], 0, v[150:151]
	v_mad_u64_u32 v[30:31], s[10:11], v28, s44, v[16:17]
	v_mad_i32_i24 v31, v29, s44, v31
	v_lshl_add_u64 v[30:31], v[30:31], 0, v[150:151]
	v_lshl_add_u64 v[34:35], s[8:9], 0, v[144:145]
	global_load_dwordx4 v[26:29], v[26:27], off
	s_nop 0
	global_load_dwordx4 v[30:33], v[30:31], off
	v_mad_u64_u32 v[36:37], s[10:11], v34, s44, v[16:17]
	v_mad_i32_i24 v37, v35, s44, v37
	v_lshl_add_u64 v[34:35], v[36:37], 0, v[152:153]
	global_load_dwordx4 v[34:37], v[34:35], off offset:256
	s_nop 0
	global_load_dwordx4 v[124:127], v[38:39], off
	global_load_dwordx4 v[120:123], v[38:39], off offset:32
	global_load_dwordx4 v[116:119], v[38:39], off offset:64
	global_load_dwordx4 v[112:115], v[38:39], off offset:96
	global_load_dwordx4 v[108:111], v[38:39], off offset:128
	global_load_dwordx4 v[104:107], v[38:39], off offset:160
	global_load_dwordx4 v[100:103], v[38:39], off offset:192
	global_load_dwordx4 v[96:99], v[38:39], off offset:224
	s_lshl_b32 s8, s12, 12
	v_add_u32_e32 v190, s8, v166
	v_add_u32_e32 v191, s45, v170
	v_add_u32_e32 v192, s45, v171
	v_add_u32_e32 v193, s45, v172
	v_add_u32_e32 v194, s45, v173
	s_mov_b32 s8, s9
	s_mov_b32 s10, s9
	s_mov_b32 s11, s9
	s_mov_b32 s12, s9
	s_mov_b32 s13, s9
	s_mov_b32 s14, s9
	s_mov_b32 s15, s9
	s_mov_b32 s16, s9
	s_mov_b32 s17, s9
	s_mov_b32 s18, s9
	s_mov_b32 s19, s9
	s_mov_b32 s20, s9
	s_mov_b32 s21, s9
	s_mov_b32 s22, s9
	s_mov_b32 s23, s9
	v_add_u32_e32 v195, 0, v168
	v_mov_b32_e32 v140, 0
	v_add_u32_e32 v196, 0x12000, v195
	v_lshrrev_b32_e32 v156, 4, v254
	v_and_b32_e32 v157, 7, v156
	v_and_b32_e32 v159, 15, v254
	v_xor_b32_e32 v157, v157, v159
	v_lshlrev_b32_e32 v157, 4, v157
	v_mad_u32_u24 v154, v156, s44, v157
	v_lshrrev_b32_e32 v156, 3, v254
	v_and_b32_e32 v157, 7, v156
	v_and_b32_e32 v159, 7, v254
	v_xor_b32_e32 v157, v157, v159
	v_lshlrev_b32_e32 v157, 4, v157
	v_add_u32_e32 v157, 0x100, v157
	v_mad_u32_u24 v155, v156, s44, v157
	v_and_b32_e32 v158, 3, v254
	v_lshlrev_b32_e32 v158, 4, v158
	v_bfe_u32 v156, v254, 5, 2
	v_lshl_or_b32 v158, v156, 6, v158
	v_bfe_u32 v156, v254, 2, 2
	v_lshl_or_b32 v158, v156, 11, v158
	v_bfe_u32 v156, v254, 7, 1
	v_lshl_or_b32 v158, v156, 13, v158
	v_bfe_u32 v156, v254, 4, 1
	v_lshl_or_b32 v158, v156, 14, v158
	v_bfe_u32 v156, v254, 8, 1
	v_lshl_or_b32 v158, v156, 15, v158
	s_waitcnt vmcnt(16)
	ds_write_b128 v190, v[0:3]
	s_waitcnt vmcnt(15)
	ds_write_b128 v190, v[4:7] offset:1024
	s_waitcnt vmcnt(14)
	ds_write_b128 v190, v[8:11] offset:2048
	s_waitcnt vmcnt(13)
	ds_write_b128 v190, v[12:15] offset:3072
	s_waitcnt vmcnt(0)
	s_waitcnt vmcnt(12)
	ds_write_b128 v175, v[18:21]
	s_waitcnt vmcnt(11)
	ds_write_b128 v176, v[22:25]
	s_waitcnt vmcnt(10)
	ds_write_b128 v177, v[26:29] offset:32768
	s_waitcnt vmcnt(9)
	ds_write_b128 v178, v[30:33] offset:32768
	s_waitcnt vmcnt(8)
	ds_write_b128 v179, v[34:37]
	s_waitcnt lgkmcnt(0)
	s_barrier
	ds_read_b128 v[0:3], v180 offset:32768
	ds_read_b128 v[4:7], v180 offset:40960
	s_waitcnt vmcnt(7) lgkmcnt(1)
	v_mfma_f32_32x32x16_bf16 v[48:63], v[0:3], v[124:127], 0
	s_waitcnt lgkmcnt(0)
	v_mfma_f32_32x32x16_bf16 v[64:79], v[4:7], v[124:127], 0
	ds_read_b128 v[0:3], v181 offset:32768
	ds_read_b128 v[4:7], v181 offset:40960
	s_waitcnt vmcnt(6) lgkmcnt(1)
	v_mfma_f32_32x32x16_bf16 v[48:63], v[0:3], v[120:123], v[48:63]
	s_waitcnt lgkmcnt(0)
	v_mfma_f32_32x32x16_bf16 v[64:79], v[4:7], v[120:123], v[64:79]
	ds_read_b128 v[0:3], v182 offset:32768
	ds_read_b128 v[4:7], v182 offset:40960
	s_waitcnt vmcnt(5) lgkmcnt(1)
	v_mfma_f32_32x32x16_bf16 v[48:63], v[0:3], v[116:119], v[48:63]
	s_waitcnt lgkmcnt(0)
	v_mfma_f32_32x32x16_bf16 v[64:79], v[4:7], v[116:119], v[64:79]
	ds_read_b128 v[0:3], v183 offset:32768
	ds_read_b128 v[4:7], v183 offset:40960
	s_waitcnt vmcnt(4) lgkmcnt(1)
	v_mfma_f32_32x32x16_bf16 v[48:63], v[0:3], v[112:115], v[48:63]
	s_waitcnt lgkmcnt(0)
	v_mfma_f32_32x32x16_bf16 v[64:79], v[4:7], v[112:115], v[64:79]
	ds_read_b128 v[0:3], v184 offset:32768
	ds_read_b128 v[4:7], v184 offset:40960
	s_waitcnt vmcnt(3) lgkmcnt(1)
	v_mfma_f32_32x32x16_bf16 v[48:63], v[0:3], v[108:111], v[48:63]
	s_waitcnt lgkmcnt(0)
	v_mfma_f32_32x32x16_bf16 v[64:79], v[4:7], v[108:111], v[64:79]
	ds_read_b128 v[0:3], v185 offset:32768
	ds_read_b128 v[4:7], v185 offset:40960
	s_waitcnt vmcnt(2) lgkmcnt(1)
	v_mfma_f32_32x32x16_bf16 v[48:63], v[0:3], v[104:107], v[48:63]
	s_waitcnt lgkmcnt(0)
	v_mfma_f32_32x32x16_bf16 v[64:79], v[4:7], v[104:107], v[64:79]
	ds_read_b128 v[0:3], v186 offset:32768
	ds_read_b128 v[4:7], v186 offset:40960
	s_waitcnt vmcnt(1) lgkmcnt(1)
	v_mfma_f32_32x32x16_bf16 v[48:63], v[0:3], v[100:103], v[48:63]
	s_waitcnt lgkmcnt(0)
	v_mfma_f32_32x32x16_bf16 v[64:79], v[4:7], v[100:103], v[64:79]
	ds_read_b128 v[0:3], v187 offset:32768
	ds_read_b128 v[4:7], v187 offset:40960
	s_waitcnt vmcnt(0) lgkmcnt(1)
	v_mfma_f32_32x32x16_bf16 v[48:63], v[0:3], v[96:99], v[48:63]
	s_waitcnt lgkmcnt(0)
	v_mfma_f32_32x32x16_bf16 v[64:79], v[4:7], v[96:99], v[64:79]
	ds_read_b128 v[0:3], v191
	ds_read_b128 v[4:7], v190
	ds_read_b128 v[8:11], v191 offset:4096
	ds_read_b128 v[12:15], v190 offset:1024
	s_waitcnt lgkmcnt(2)
	v_mfma_f32_32x32x16_bf16 v[48:63], v[0:3], v[4:7], v[48:63]
	s_waitcnt lgkmcnt(1)
	v_mfma_f32_32x32x16_bf16 v[64:79], v[8:11], v[4:7], v[64:79]
	ds_read_b128 v[0:3], v192
	ds_read_b128 v[4:7], v192 offset:4096
	s_waitcnt lgkmcnt(1)
	v_mfma_f32_32x32x16_bf16 v[48:63], v[0:3], v[12:15], v[48:63]
	s_waitcnt lgkmcnt(0)
	v_mfma_f32_32x32x16_bf16 v[64:79], v[4:7], v[12:15], v[64:79]
	ds_read_b128 v[0:3], v193
	ds_read_b128 v[4:7], v190 offset:2048
	ds_read_b128 v[8:11], v193 offset:4096
	ds_read_b128 v[18:21], v190 offset:3072
	ds_read_b128 v[22:25], v194 offset:4096
	s_waitcnt lgkmcnt(3)
	v_mfma_f32_32x32x16_bf16 v[48:63], v[0:3], v[4:7], v[48:63]
	ds_read_b128 v[0:3], v194
	s_waitcnt lgkmcnt(3)
	v_mfma_f32_32x32x16_bf16 v[64:79], v[8:11], v[4:7], v[64:79]
	s_waitcnt lgkmcnt(0)
	v_mfma_f32_32x32x16_bf16 v[48:63], v[0:3], v[18:21], v[48:63]
	v_mov_b64_e32 v[0:1], s[8:9]
	v_mov_b64_e32 v[2:3], s[10:11]
	v_mov_b64_e32 v[4:5], s[12:13]
	v_mov_b64_e32 v[6:7], s[14:15]
	v_mov_b64_e32 v[8:9], s[16:17]
	v_mov_b64_e32 v[10:11], s[18:19]
	v_mov_b64_e32 v[12:13], s[20:21]
	v_mfma_f32_32x32x16_bf16 v[64:79], v[22:25], v[18:21], v[64:79]
	s_nop 3
	v_max_f32_e32 v18, v49, v49
	v_max_f32_e32 v19, v48, v48
	v_max_f32_e32 v18, v19, v18
	v_max3_f32 v18, v18, v50, v51
	v_max3_f32 v18, v18, v52, v53
	v_max3_f32 v18, v18, v54, v55
	v_max3_f32 v18, v18, v56, v57
	v_max3_f32 v18, v18, v58, v59
	v_max3_f32 v18, v18, v60, v61
	v_max3_f32 v18, v18, v62, v63
	v_max3_f32 v18, v18, v64, v65
	v_max3_f32 v18, v18, v66, v67
	v_max3_f32 v18, v18, v68, v69
	v_max3_f32 v18, v18, v70, v71
	v_max3_f32 v18, v18, v72, v73
	v_max3_f32 v18, v18, v74, v75
	v_max3_f32 v18, v18, v76, v77
	v_max3_f32 v18, v18, v78, v79
	v_mov_b32_e32 v19, v18
	s_nop 1
	v_permlane32_swap_b32_e32 v18, v19
	v_mov_b64_e32 v[14:15], s[22:23]
	s_and_b32 s8, s62, 0x3fffffc0
	v_max_f32_e32 v19, v19, v19
	v_max_f32_e32 v18, v18, v18
	s_lshl_b32 s8, s8, 2
	v_max_f32_e32 v18, v18, v19
	s_add_i32 s12, s8, 0
	v_add_f32_e32 v19, 0x7149f2ca, v18
	s_add_i32 s12, s12, 0x14000
	v_cmp_ge_f32_e32 vcc, s46, v19
	s_cmp_eq_u64 vcc, exec
	s_cselect_b64 vcc, -1, 0
	s_add_i32 s8, s60, 0x4040
	v_max_f32_e32 v128, 0xf149f2ca, v18
	v_lshl_add_u64 v[18:19], s[8:9], 0, v[142:143]
	v_lshl_add_u64 v[20:21], v[146:147], 0, s[8:9]
	v_lshl_add_u64 v[22:23], s[8:9], 0, v[144:145]
	v_lshlrev_b64 v[24:25], 11, v[18:19]
	v_lshlrev_b64 v[26:27], 11, v[20:21]
	v_mad_u64_u32 v[28:29], s[10:11], v18, s44, v[16:17]
	v_mad_u64_u32 v[30:31], s[10:11], v20, s44, v[16:17]
	v_mad_u64_u32 v[16:17], s[10:11], v22, s44, v[16:17]
	v_lshl_add_u64 v[24:25], s[30:31], 0, v[24:25]
	v_lshl_add_u64 v[26:27], s[30:31], 0, v[26:27]
	v_mad_i32_i24 v29, v19, s44, v29
	v_mad_i32_i24 v31, v21, s44, v31
	v_mad_i32_i24 v17, v23, s44, v17
	v_lshl_add_u64 v[18:19], v[24:25], 0, v[150:151]
	v_lshl_add_u64 v[20:21], v[26:27], 0, v[150:151]
	v_lshl_add_u64 v[22:23], v[28:29], 0, v[150:151]
	v_lshl_add_u64 v[24:25], v[30:31], 0, v[150:151]
	v_lshl_add_u64 v[16:17], v[16:17], 0, v[152:153]
	global_load_dwordx4 v[80:83], v[18:19], off
	global_load_dwordx4 v[84:87], v[20:21], off
	global_load_dwordx4 v[88:91], v[22:23], off
	global_load_dwordx4 v[92:95], v[24:25], off
	global_load_dwordx4 v[200:203], v[16:17], off offset:256
	v_sub_f32_e32 v129, 0xf149f2ca, v128
	v_mul_f32_e32 v129, 0x3dd53b94, v129
	v_exp_f32_e32 v164, v129
	v_mov_b32_e32 v129, 0xf149f2ca
	v_cndmask_b32_e32 v198, v128, v129, vcc
	v_mul_f32_e32 v138, 0xbdd53b94, v198
	v_mov_b32_e32 v165, v138
	v_fmamk_f32 v48, v48, 0x3dd53b94, v138
	v_fmamk_f32 v49, v49, 0x3dd53b94, v138
	v_fmamk_f32 v50, v50, 0x3dd53b94, v138
	v_fmamk_f32 v51, v51, 0x3dd53b94, v138
	v_fmamk_f32 v52, v52, 0x3dd53b94, v138
	v_fmamk_f32 v53, v53, 0x3dd53b94, v138
	v_fmamk_f32 v54, v54, 0x3dd53b94, v138
	v_fmamk_f32 v55, v55, 0x3dd53b94, v138
	v_fmamk_f32 v56, v56, 0x3dd53b94, v138
	v_fmamk_f32 v57, v57, 0x3dd53b94, v138
	v_fmamk_f32 v58, v58, 0x3dd53b94, v138
	v_fmamk_f32 v59, v59, 0x3dd53b94, v138
	v_fmamk_f32 v60, v60, 0x3dd53b94, v138
	v_fmamk_f32 v61, v61, 0x3dd53b94, v138
	v_fmamk_f32 v62, v62, 0x3dd53b94, v138
	v_fmac_f32_e32 v165, 0x3dd53b94, v63
	v_exp_f32_e32 v222, v48
	v_exp_f32_e32 v224, v49
	v_exp_f32_e32 v220, v50
	v_exp_f32_e32 v223, v51
	v_exp_f32_e32 v219, v52
	v_exp_f32_e32 v221, v53
	v_exp_f32_e32 v217, v54
	v_exp_f32_e32 v218, v55
	v_exp_f32_e32 v212, v56
	v_exp_f32_e32 v214, v57
	v_exp_f32_e32 v211, v58
	v_exp_f32_e32 v213, v59
	v_exp_f32_e32 v208, v60
	v_exp_f32_e32 v210, v61
	v_exp_f32_e32 v207, v62
	v_exp_f32_e32 v209, v165
	s_waitcnt vmcnt(0)
	v_mov_b64_e32 v[46:47], v[14:15]
	v_mov_b64_e32 v[30:31], v[14:15]
	v_mov_b64_e32 v[62:63], v[14:15]
	s_mov_b32 s8, -1
	v_mov_b64_e32 v[44:45], v[12:13]
	v_mov_b64_e32 v[42:43], v[10:11]
	v_mov_b64_e32 v[40:41], v[8:9]
	v_mov_b64_e32 v[38:39], v[6:7]
	v_mov_b64_e32 v[36:37], v[4:5]
	v_mov_b64_e32 v[34:35], v[2:3]
	v_mov_b64_e32 v[32:33], v[0:1]
	v_mov_b64_e32 v[28:29], v[12:13]
	v_mov_b64_e32 v[26:27], v[10:11]
	v_mov_b64_e32 v[24:25], v[8:9]
	v_mov_b64_e32 v[22:23], v[6:7]
	v_mov_b64_e32 v[20:21], v[4:5]
	v_mov_b64_e32 v[18:19], v[2:3]
	v_mov_b64_e32 v[16:17], v[0:1]
	v_lshl_add_u32 v189, v188, 2, s12
	s_add_i32 s13, s60, 0x4080
	s_add_i32 s83, s60, 0x4040
	s_sub_i32 s14, s61, 64
	v_pk_fma_f32 v[134:135], v[78:79], s[26:27], v[138:139] op_sel_hi:[1,0,0]
	v_pk_fma_f32 v[160:161], v[76:77], s[26:27], v[138:139] op_sel_hi:[1,0,0]
	v_pk_fma_f32 v[162:163], v[74:75], s[26:27], v[138:139] op_sel_hi:[1,0,0]
	v_pk_fma_f32 v[128:129], v[72:73], s[26:27], v[138:139] op_sel_hi:[1,0,0]
	v_pk_fma_f32 v[130:131], v[70:71], s[26:27], v[138:139] op_sel_hi:[1,0,0]
	v_pk_fma_f32 v[132:133], v[68:69], s[26:27], v[138:139] op_sel_hi:[1,0,0]
	v_pk_fma_f32 v[136:137], v[66:67], s[26:27], v[138:139] op_sel_hi:[1,0,0]
	v_pk_fma_f32 v[138:139], v[64:65], s[26:27], v[138:139] op_sel_hi:[1,0,0]
	v_cndmask_b32_e64 v197, v164, 1.0, vcc
	v_mov_b64_e32 v[60:61], v[12:13]
	v_mov_b64_e32 v[58:59], v[10:11]
	v_mov_b64_e32 v[56:57], v[8:9]
	v_mov_b64_e32 v[54:55], v[6:7]
	v_mov_b64_e32 v[52:53], v[4:5]
	v_mov_b64_e32 v[50:51], v[2:3]
	v_mov_b64_e32 v[48:49], v[0:1]
	s_waitcnt vmcnt(4)
	ds_write_b128 v175, v[80:83] offset:16384
	s_waitcnt vmcnt(3)
	ds_write_b128 v176, v[84:87] offset:16384
	s_waitcnt vmcnt(2)
	ds_write_b128 v177, v[88:91] offset:49152
	s_waitcnt vmcnt(1)
	ds_write_b128 v178, v[92:95] offset:49152
	s_waitcnt vmcnt(0)
	ds_write_b128 v196, v[200:203]
	s_waitcnt lgkmcnt(0)
	s_barrier
	.p2align	6
